# speedup vs baseline: 1.1325x; 1.0027x over previous
.LBB1_8:
	s_lshl_b32 s2, s36, 2
	s_add_i32 s24, s2, s15
	s_add_i32 s38, s36, 1
	s_cmp_lt_i32 s38, s35
	s_cselect_b64 s[22:23], -1, 0
	s_cmp_ge_i32 s38, s35
	s_cbranch_scc1 .LBB1_10
	s_lshl_b32 s2, s24, 4
	v_add_u32_e32 v2, s2, v150
	v_add_u32_e32 v4, s2, v153
	v_add_u32_e32 v74, s2, v154
	v_add_u32_e32 v76, s2, v155
	v_min_i32_e32 v2, 0xc34f, v2
	v_min_i32_e32 v4, 0xc34f, v4
	v_min_i32_e32 v74, 0xc34f, v74
	v_min_i32_e32 v76, 0xc34f, v76
	v_ashrrev_i32_e32 v3, 31, v2
	v_ashrrev_i32_e32 v5, 31, v4
	v_ashrrev_i32_e32 v75, 31, v74
	v_ashrrev_i32_e32 v77, 31, v76
	v_lshlrev_b64 v[2:3], 9, v[2:3]
	v_lshlrev_b64 v[4:5], 9, v[4:5]
	v_lshlrev_b64 v[74:75], 9, v[74:75]
	v_lshlrev_b64 v[76:77], 9, v[76:77]
	v_lshl_add_u64 v[2:3], v[128:129], 0, v[2:3]
	v_lshl_add_u64 v[6:7], v[128:129], 0, v[4:5]
	v_lshl_add_u64 v[74:75], v[128:129], 0, v[74:75]
	v_lshl_add_u64 v[78:79], v[128:129], 0, v[76:77]
	global_load_dwordx4 v[2:5], v[2:3], off
	s_nop 0
	global_load_dwordx4 v[6:9], v[6:7], off
	s_nop 0
	global_load_dwordx4 v[74:77], v[74:75], off
	s_nop 0
	global_load_dwordx4 v[78:81], v[78:79], off

.LBB1_42:
	s_cmp_eq_u32 s36, 1
	s_cbranch_scc0 .LBB1_47
	ds_add_rtn_u32 v94, v167, v223
	ds_add_rtn_u32 v95, v171, v223
	ds_add_rtn_u32 v96, v175, v223
	ds_add_rtn_u32 v97, v179, v223
	ds_add_rtn_u32 v98, v183, v223
	ds_add_rtn_u32 v99, v187, v223
	ds_add_rtn_u32 v100, v191, v223
	ds_add_rtn_u32 v101, v195, v223
	ds_add_rtn_u32 v102, v199, v223
	ds_add_rtn_u32 v103, v203, v223
	ds_add_rtn_u32 v104, v207, v223
	v_mov_b32_e32 v122, 0x16400
	v_mov_b32_e32 v123, 0x1c5c0
	s_waitcnt lgkmcnt(0)
	ds_read_b32 v105, v169
	ds_read_b32 v106, v170
	ds_read_b32 v107, v173
	ds_read_b32 v108, v174
	ds_read_b32 v109, v177
	ds_read_b32 v110, v178
	ds_read_b32 v111, v181
	ds_read_b32 v112, v182
	ds_read_b32 v113, v185
	ds_read_b32 v114, v186
	ds_read_b32 v115, v189
	ds_read_b32 v116, v190
	ds_read_b32 v117, v193
	ds_read_b32 v118, v194
	s_waitcnt lgkmcnt(0)
	v_lshl_add_u32 v119, v94, 2, v122
	ds_write_b32 v119, v168
	v_add_u32_e32 v120, v105, v94
	v_lshl_add_u32 v121, v94, 2, v123
	v_sub_u32_e32 v120, v120, v106
	ds_write_b32 v121, v120
	v_lshl_add_u32 v119, v95, 2, v122
	ds_write_b32 v119, v172
	v_add_u32_e32 v120, v107, v95
	v_lshl_add_u32 v121, v95, 2, v123
	v_sub_u32_e32 v120, v120, v108
	ds_write_b32 v121, v120
	v_lshl_add_u32 v119, v96, 2, v122
	ds_write_b32 v119, v176
	v_add_u32_e32 v120, v109, v96
	v_lshl_add_u32 v121, v96, 2, v123
	v_sub_u32_e32 v120, v120, v110
	ds_write_b32 v121, v120
	v_lshl_add_u32 v119, v97, 2, v122
	ds_write_b32 v119, v180
	v_add_u32_e32 v120, v111, v97
	v_lshl_add_u32 v121, v97, 2, v123
	v_sub_u32_e32 v120, v120, v112
	ds_write_b32 v121, v120
	v_lshl_add_u32 v119, v98, 2, v122
	ds_write_b32 v119, v184
	v_add_u32_e32 v120, v113, v98
	v_lshl_add_u32 v121, v98, 2, v123
	v_sub_u32_e32 v120, v120, v114
	ds_write_b32 v121, v120
	v_lshl_add_u32 v119, v99, 2, v122
	ds_write_b32 v119, v188
	v_add_u32_e32 v120, v115, v99
	v_lshl_add_u32 v121, v99, 2, v123
	v_sub_u32_e32 v120, v120, v116
	ds_write_b32 v121, v120
	v_lshl_add_u32 v119, v100, 2, v122
	ds_write_b32 v119, v192
	v_add_u32_e32 v120, v117, v100
	v_lshl_add_u32 v121, v100, 2, v123
	v_sub_u32_e32 v120, v120, v118
	ds_write_b32 v121, v120
	s_waitcnt lgkmcnt(0)
	ds_read_b32 v105, v197
	ds_read_b32 v106, v198
	ds_read_b32 v107, v201
	ds_read_b32 v108, v202
	ds_read_b32 v109, v205
	ds_read_b32 v110, v206
	ds_read_b32 v111, v209
	ds_read_b32 v112, v210
	s_waitcnt lgkmcnt(0)
	v_lshl_add_u32 v119, v101, 2, v122
	ds_write_b32 v119, v196
	v_add_u32_e32 v120, v105, v101
	v_lshl_add_u32 v121, v101, 2, v123
	v_sub_u32_e32 v120, v120, v106
	ds_write_b32 v121, v120
	v_lshl_add_u32 v119, v102, 2, v122
	ds_write_b32 v119, v200
	v_add_u32_e32 v120, v107, v102
	v_lshl_add_u32 v121, v102, 2, v123
	v_sub_u32_e32 v120, v120, v108
	ds_write_b32 v121, v120
	v_lshl_add_u32 v119, v103, 2, v122
	ds_write_b32 v119, v204
	v_add_u32_e32 v120, v109, v103
	v_lshl_add_u32 v121, v103, 2, v123
	v_sub_u32_e32 v120, v120, v110
	ds_write_b32 v121, v120
	v_lshl_add_u32 v119, v104, 2, v122
	ds_write_b32 v119, v208
	v_add_u32_e32 v120, v111, v104
	v_lshl_add_u32 v121, v104, 2, v123
	v_sub_u32_e32 v120, v120, v112
	ds_write_b32 v121, v120
	s_and_saveexec_b64 s[2:3], s[0:1]
	s_cbranch_execz .LBB1_46
	ds_add_rtn_u32 v94, v211, v223
	s_waitcnt lgkmcnt(0)
	v_lshlrev_b32_e32 v95, 2, v94
	v_add_u32_e32 v96, 0x16400, v95
	ds_write_b32 v96, v212
	ds_read_b32 v96, v213
	ds_read_b32 v97, v214
	v_add_u32_e32 v95, 0x1c5c0, v95
	s_waitcnt lgkmcnt(1)
	v_add_u32_e32 v94, v96, v94
	s_waitcnt lgkmcnt(0)
	v_sub_u32_e32 v94, v94, v97
	ds_write_b32 v95, v94
	s_and_b64 exec, exec, s[10:11]
	s_cbranch_execz .LBB1_46
	ds_add_rtn_u32 v94, v216, v223
	s_waitcnt lgkmcnt(0)
	v_lshlrev_b32_e32 v95, 2, v94
	v_add_u32_e32 v96, 0x16400, v95
	ds_write_b32 v96, v217
	ds_read_b32 v96, v218
	ds_read_b32 v97, v219
	v_add_u32_e32 v95, 0x1c5c0, v95
	s_waitcnt lgkmcnt(1)
	v_add_u32_e32 v94, v96, v94
	s_waitcnt lgkmcnt(0)
	v_sub_u32_e32 v94, v94, v97
	ds_write_b32 v95, v94

.LBB1_59:
	s_and_saveexec_b64 s[0:1], s[12:13]
	s_cbranch_execz .LBB1_62
	v_mbcnt_hi_u32_b32 v2, -1, v148
	v_and_b32_e32 v3, 64, v2
	v_xor_b32_e32 v1, 16, v2
	v_add_u32_e32 v3, 64, v3
	v_cmp_lt_i32_e32 vcc, v1, v3
	v_xor_b32_e32 v5, 32, v2
	v_max_f32_e32 v4, v215, v215
	v_cndmask_b32_e32 v1, v2, v1, vcc
	v_lshlrev_b32_e32 v1, 2, v1
	ds_bpermute_b32 v1, v1, v215
	v_cmp_lt_i32_e32 vcc, v5, v3
	s_waitcnt lgkmcnt(0)
	v_max_f32_e32 v1, v1, v1
	v_cndmask_b32_e32 v2, v2, v5, vcc
	v_max_f32_e32 v1, v4, v1
	v_lshlrev_b32_e32 v2, 2, v2
	ds_bpermute_b32 v2, v2, v1
	v_cmp_eq_u32_e32 vcc, 0, v143
	s_and_b64 exec, exec, vcc
	s_cbranch_execz .LBB1_62
	s_waitcnt lgkmcnt(0)
	v_max_f32_e32 v2, v2, v2
	v_max_f32_e32 v1, v1, v1
	v_max_f32_e32 v1, v1, v2
	v_not_b32_e32 v2, v1
	v_or_b32_e32 v3, 0x80000000, v1
	v_cmp_gt_i32_e32 vcc, 0, v1
	s_nop 1
	v_cndmask_b32_e32 v1, v3, v2, vcc
	v_lshlrev_b32_e32 v2, 2, v146
	global_atomic_umax v2, v1, s[28:29]
.LBB1_62:
	s_or_b64 exec, exec, s[0:1]
	v_add_u32_e32 v1, 0x1c5c0, v142
	s_waitcnt lgkmcnt(0)
	s_barrier
	ds_read2st64_b32 v[4:5], v1 offset1:8
	v_add_u32_e32 v2, 0x16400, v142
	ds_read2st64_b32 v[6:7], v2 offset1:8
	s_mul_i32 s0, s14, 0x30d400
	s_mul_hi_i32 s1, s14, 0x30d400
	s_add_u32 s0, s26, s0
	s_addc_u32 s1, s27, s1
	s_waitcnt lgkmcnt(1)
	v_ashrrev_i32_e32 v9, 31, v4
	v_mov_b32_e32 v8, v4
	v_lshl_add_u64 v[8:9], v[8:9], 2, s[0:1]
	s_waitcnt lgkmcnt(0)
	global_store_dword v[8:9], v6, off
	v_ashrrev_i32_e32 v9, 31, v5
	v_mov_b32_e32 v8, v5
	v_lshl_add_u64 v[4:5], v[8:9], 2, s[0:1]
	global_store_dword v[4:5], v7, off
	ds_read2st64_b32 v[4:5], v1 offset0:24 offset1:40
	v_add_u32_e32 v3, 0x17400, v142
	v_add_u32_e32 v6, 0x1d5c0, v142
	v_add_u32_e32 v8, 0x1e5c0, v142
	v_add_u32_e32 v10, 0x1f5c0, v142
	v_add_u32_e32 v12, 0x205c0, v142
	v_add_u32_e32 v7, 0x18400, v142
	v_add_u32_e32 v9, 0x19400, v142
	v_add_u32_e32 v11, 0x1a400, v142
	ds_read_b32 v3, v3
	ds_read_b32 v6, v6
	ds_read_b32 v13, v7
	ds_read_b32 v8, v8
	ds_read_b32 v16, v9
	ds_read_b32 v10, v10
	ds_read_b32 v17, v11
	ds_read_b32 v12, v12
	ds_read2st64_b32 v[14:15], v2 offset0:24 offset1:40
	s_waitcnt lgkmcnt(7)
	v_ashrrev_i32_e32 v7, 31, v6
	v_lshl_add_u64 v[6:7], v[6:7], 2, s[0:1]
	global_store_dword v[6:7], v3, off
	v_ashrrev_i32_e32 v7, 31, v4
	v_mov_b32_e32 v6, v4
	v_lshl_add_u64 v[6:7], v[6:7], 2, s[0:1]
	s_waitcnt lgkmcnt(5)
	v_ashrrev_i32_e32 v9, 31, v8
	s_waitcnt lgkmcnt(0)
	global_store_dword v[6:7], v14, off
	v_lshl_add_u64 v[6:7], v[8:9], 2, s[0:1]
	global_store_dword v[6:7], v13, off
	v_ashrrev_i32_e32 v7, 31, v5
	v_mov_b32_e32 v6, v5
	v_lshl_add_u64 v[4:5], v[6:7], 2, s[0:1]
	global_store_dword v[4:5], v15, off
	ds_read2st64_b32 v[4:5], v1 offset0:56 offset1:72
	ds_read2st64_b32 v[8:9], v2 offset0:56 offset1:72
	v_ashrrev_i32_e32 v11, 31, v10
	v_lshl_add_u64 v[6:7], v[10:11], 2, s[0:1]
	global_store_dword v[6:7], v16, off
	s_waitcnt lgkmcnt(1)
	v_ashrrev_i32_e32 v7, 31, v4
	v_mov_b32_e32 v6, v4
	v_lshl_add_u64 v[6:7], v[6:7], 2, s[0:1]
	v_ashrrev_i32_e32 v13, 31, v12
	s_waitcnt lgkmcnt(0)
	global_store_dword v[6:7], v8, off
	v_lshl_add_u64 v[6:7], v[12:13], 2, s[0:1]
	global_store_dword v[6:7], v17, off
	v_add_u32_e32 v3, 0x1b400, v142
	v_add_u32_e32 v4, 0x215c0, v142
	ds_read_b32 v3, v3
	ds_read_b32 v4, v4
	v_ashrrev_i32_e32 v7, 31, v5
	v_mov_b32_e32 v6, v5
	s_movk_i32 s2, 0x26a
	v_lshl_add_u64 v[6:7], v[6:7], 2, s[0:1]
	s_waitcnt lgkmcnt(0)
	v_ashrrev_i32_e32 v5, 31, v4
	v_lshl_add_u64 v[4:5], v[4:5], 2, s[0:1]
	v_cmp_gt_u32_e32 vcc, s2, v0
	global_store_dword v[6:7], v9, off
	global_store_dword v[4:5], v3, off
	s_and_saveexec_b64 s[2:3], vcc
	s_cbranch_execz .LBB1_64
	ds_read_b32 v4, v1 offset:22528
	ds_read_b32 v1, v2 offset:22528
	s_waitcnt lgkmcnt(1)
	v_ashrrev_i32_e32 v5, 31, v4
	v_lshl_add_u64 v[2:3], v[4:5], 2, s[0:1]
	s_waitcnt lgkmcnt(0)
	global_store_dword v[2:3], v1, off

.Lagg_scatter_done:
	s_lshl_b32 s52, s3, 7
	s_add_u32 s52, s18, s52
	s_addc_u32 s53, s19, 0
	v_lshlrev_b32_e32 v40, 1, v1
	global_load_dwordx4 v[16:19], v40, s[52:53]
	global_load_dwordx4 v[20:23], v40, s[52:53] offset:16
	global_load_dword v56, v13, s[20:21] offset:0
	global_load_dword v57, v13, s[20:21] offset:16
	s_waitcnt lgkmcnt(0)
	s_barrier
	v_lshrrev_b32_e32 v40, 6, v0
	s_nop 0
	v_readfirstlane_b32 s41, v40
	s_cmp_gt_u32 s41, 12
	s_cbranch_scc1 .Lagg_exit
	v_mov_b32_e32 v15, 1.0
	s_lshl_b32 s52, s3, 8
	s_add_u32 s68, s30, s52
	s_addc_u32 s69, s31, 0
	s_mul_i32 s52, s3, 0x61a800
	s_add_u32 s70, s14, s52
	s_addc_u32 s71, s15, 0
	s_mul_i32 s52, s3, 0x61a800
	s_add_u32 s48, s12, s52
	s_addc_u32 s49, s13, 0
	s_waitcnt vmcnt(0)
	v_not_b32_e32 v58, v56
	v_and_b32_e32 v59, 0x7fffffff, v56
	v_cmp_gt_i32_e32 vcc, 0, v56
	s_nop 1
	v_cndmask_b32_e32 v56, v58, v59, vcc
	v_not_b32_e32 v58, v57
	v_and_b32_e32 v59, 0x7fffffff, v57
	v_cmp_gt_i32_e32 vcc, 0, v57
	s_nop 1
	v_cndmask_b32_e32 v57, v58, v59, vcc
	v_mov_b32_e32 v46, v56
	v_add_f32_e32 v14, v56, v57
	v_mul_f32_e32 v58, 0x3c23d70a, v14
	v_max_f32_e32 v14, v14, v58
	s_cmp_eq_u32 s7, 0
	s_cbranch_scc1 .Lagg_slow_0
	s_lshl_b32 s40, s41, 4
	v_bfe_u32 v63, v0, 2, 4
	v_add_u32_e32 v63, s40, v63
	v_cmp_gt_u32_e32 vcc, 0xc4, v63
	s_and_saveexec_b64 s[58:59], vcc
	s_cbranch_execz .Lagg_phasedone_0_0
	v_lshlrev_b32_e32 v63, 1, v63
	ds_read_u16 v60, v63 offset:18432
	v_lshrrev_b32_e32 v63, 2, v1
	s_waitcnt lgkmcnt(0)
	v_lshlrev_b32_e32 v61, 2, v60
	ds_read_b32 v58, v61 offset:14336
	ds_read_b32 v59, v61 offset:14340
	v_add_u32_e32 v57, s6, v60
	v_min_u32_e32 v57, 0xc34f, v57
	v_lshlrev_b32_e32 v57, 6, v57
	v_add3_u32 v57, v57, v13, 16
	global_load_dword v57, v57, s[16:17] offset:0
	v_lshl_add_u32 v61, v60, 4, v63
	v_mov_b32_e32 v45, 0
	v_mov_b32_e32 v48, 0
	v_mov_b32_e32 v49, 0
	v_mov_b32_e32 v50, 0
	v_mov_b32_e32 v51, 0
	v_mov_b32_e32 v52, 0
	v_mov_b32_e32 v53, 0
	v_mov_b32_e32 v54, 0
	v_mov_b32_e32 v55, 0
	s_waitcnt lgkmcnt(0)
	v_lshlrev_b32_e32 v41, 1, v58
	v_lshlrev_b32_e32 v42, 1, v59
	v_cmp_lt_u32_e32 vcc, v41, v42
	s_and_saveexec_b64 s[64:65], vcc
	s_cbranch_execz .Lagg_listdone_0_0
	ds_read_u16 v40, v41
	v_add_u32_e32 v41, 2, v41
	s_waitcnt lgkmcnt(0)
	v_mad_u32_u16 v24, v40, s46, v1
	global_load_dwordx4 v[28:31], v24, s[48:49] offset:64
	global_load_dwordx4 v[24:27], v24, s[48:49]
	s_waitcnt vmcnt(2)
	v_add_f32_e32 v47, v46, v57
	v_mul_f32_e32 v56, 0x3c23d70a, v47
	v_max_f32_e32 v47, v47, v56
	v_sub_f32_e32 v43, v57, v47
	v_mul_f32_e32 v43, 0.5, v43
	v_mul_f32_e32 v44, 0xbf7d70a4, v47

.Lagg_join_0:
	s_waitcnt vmcnt(0) lgkmcnt(0)
	s_barrier
	s_lshl_b32 s52, s3, 7
	s_add_u32 s52, s52, 0x100
	s_add_u32 s52, s18, s52
	s_addc_u32 s53, s19, 0
	v_lshlrev_b32_e32 v40, 1, v1
	global_load_dwordx4 v[16:19], v40, s[52:53]
	global_load_dwordx4 v[20:23], v40, s[52:53] offset:16
	global_load_dword v43, v13, s[20:21] offset:32
	global_load_dword v44, v13, s[20:21] offset:48
	v_cmp_gt_u32_e32 vcc, s5, v2
	s_and_saveexec_b64 s[58:59], vcc
	v_lshlrev_b32_e32 v61, 2, v0
	v_add_u32_e32 v60, 0x6e40, v61
	ds_read_b32 v48, v61 offset:21248
	ds_read_b32 v49, v61 offset:24384
	ds_read_b32 v50, v61 offset:27520
	ds_read_b32 v51, v61 offset:30656
	ds_read_b32 v52, v61 offset:33792
	ds_read_b32 v53, v61 offset:36928
	ds_read_b32 v54, v61 offset:40064
	ds_read_b32 v55, v61 offset:43200
	ds_read_b32 v45, v61 offset:46336
	s_waitcnt lgkmcnt(0)
	ds_read_b32 v24, v60 offset:21248
	ds_read_b32 v25, v60 offset:24384
	ds_read_b32 v26, v60 offset:27520
	ds_read_b32 v27, v60 offset:30656
	ds_read_b32 v28, v60 offset:33792
	ds_read_b32 v29, v60 offset:36928
	ds_read_b32 v30, v60 offset:40064
	ds_read_b32 v31, v60 offset:43200
	ds_read_b32 v32, v60 offset:46336
	v_mov_b32_e32 v62, 0x3c003c00
	s_waitcnt lgkmcnt(0)
	s_barrier
	v_pk_fma_f16 v48, v24, v62, v48
	v_pk_fma_f16 v49, v25, v62, v49
	v_pk_fma_f16 v50, v26, v62, v50
	v_pk_fma_f16 v51, v27, v62, v51
	v_pk_fma_f16 v52, v28, v62, v52
	v_pk_fma_f16 v53, v29, v62, v53
	v_pk_fma_f16 v54, v30, v62, v54
	v_pk_fma_f16 v55, v31, v62, v55
	v_add_f32_e32 v45, v45, v32
	s_cbranch_execz .Lagg_end_0
	v_add_f32_e32 v47, v46, v3
	v_mul_f32_e32 v58, 0x3c23d70a, v47
	v_max_f32_e32 v47, v47, v58
	v_sub_f32_e32 v58, v14, v47
	v_exp_f32_e32 v58, v58
	v_mul_f32_e32 v59, 0x33000000, v45
	v_rcp_f32_e32 v42, v45
	v_mul_f32_e32 v58, 0x24e69595, v58
	v_fma_f32 v60, -v45, v42, 1.0
	v_cmp_ge_f32_e64 s[62:63], v59, v58
	v_cmp_eq_f32_e32 vcc, 0, v45
	v_fmac_f32_e32 v42, v60, v42
	s_nop 1
	v_cndmask_b32_e64 v42, v42, 0, vcc
	s_or_b64 s[62:63], s[62:63], vcc
	s_mov_b64 s[66:67], exec
	s_andn2_b64 exec, exec, s[62:63]
	s_cbranch_execnz .Lagg_gmax_0

.Lagg_end_0:
	s_mov_b64 exec, s[58:59]
	s_mul_i32 s52, s3, 0x61a800
	s_add_u32 s52, s52, 0xc35000
	s_add_u32 s48, s12, s52
	s_addc_u32 s49, s13, 0
	s_waitcnt vmcnt(0)
	v_mov_b32_e32 v56, v43
	v_mov_b32_e32 v57, v44
	v_not_b32_e32 v58, v56
	v_and_b32_e32 v59, 0x7fffffff, v56
	v_cmp_gt_i32_e32 vcc, 0, v56
	s_nop 1
	v_cndmask_b32_e32 v56, v58, v59, vcc
	v_not_b32_e32 v58, v57
	v_and_b32_e32 v59, 0x7fffffff, v57
	v_cmp_gt_i32_e32 vcc, 0, v57
	s_nop 1
	v_cndmask_b32_e32 v57, v58, v59, vcc
	v_mov_b32_e32 v46, v56
	v_add_f32_e32 v14, v56, v57
	v_mul_f32_e32 v58, 0x3c23d70a, v14
	v_max_f32_e32 v14, v14, v58
	s_cmp_eq_u32 s7, 0
	s_cbranch_scc1 .Lagg_slow_1
	s_sub_u32 s40, 12, s41
	s_lshl_b32 s40, s40, 4
	v_bfe_u32 v63, v0, 2, 4
	v_add_u32_e32 v63, s40, v63
	v_cmp_gt_u32_e32 vcc, 0xc4, v63
	s_and_saveexec_b64 s[58:59], vcc
	s_cbranch_execz .Lagg_phasedone_1_0
	v_lshlrev_b32_e32 v63, 1, v63
	ds_read_u16 v60, v63 offset:19216
	v_lshrrev_b32_e32 v63, 2, v1
	s_waitcnt lgkmcnt(0)
	v_lshlrev_b32_e32 v61, 2, v60
	ds_read_b32 v58, v61 offset:16384
	ds_read_b32 v59, v61 offset:16388
	v_add_u32_e32 v57, s6, v60
	v_min_u32_e32 v57, 0xc34f, v57
	v_lshlrev_b32_e32 v57, 6, v57
	v_add3_u32 v57, v57, v13, 16
	global_load_dword v57, v57, s[16:17] offset:32
	v_lshl_add_u32 v61, v60, 4, v63
	v_mov_b32_e32 v45, 0
	v_mov_b32_e32 v48, 0
	v_mov_b32_e32 v49, 0
	v_mov_b32_e32 v50, 0
	v_mov_b32_e32 v51, 0
	v_mov_b32_e32 v52, 0
	v_mov_b32_e32 v53, 0
	v_mov_b32_e32 v54, 0
	v_mov_b32_e32 v55, 0
	s_waitcnt lgkmcnt(0)
	v_lshlrev_b32_e32 v41, 1, v58
	v_lshlrev_b32_e32 v42, 1, v59
	v_add_u32_e32 v41, 0x1c00, v41
	v_add_u32_e32 v42, 0x1c00, v42
	v_cmp_lt_u32_e32 vcc, v41, v42
	s_and_saveexec_b64 s[64:65], vcc
	s_cbranch_execz .Lagg_listdone_1_0
	ds_read_u16 v40, v41
	v_add_u32_e32 v41, 2, v41
	s_waitcnt lgkmcnt(0)
	v_mad_u32_u16 v24, v40, s46, v1
	global_load_dwordx4 v[28:31], v24, s[48:49] offset:64
	global_load_dwordx4 v[24:27], v24, s[48:49]
	s_waitcnt vmcnt(2)
	v_add_f32_e32 v47, v46, v57
	v_mul_f32_e32 v56, 0x3c23d70a, v47
	v_max_f32_e32 v47, v47, v56
	v_sub_f32_e32 v43, v57, v47
	v_mul_f32_e32 v43, 0.5, v43
	v_mul_f32_e32 v44, 0xbf7d70a4, v47
